# v94 + P8 epilogue: rolling window of 5 row groups (20 residual loads) in flight in dead VGPRs instead of 32 dependent HBM round trips per unit behind each store; compiler arithmetic kept
# speedup vs baseline: 1.0139x; 1.0003x over previous
; __device__ __forceinline__ int fresh_lane() { int l; asm volatile("v_mbcnt_lo_u32_b32 %0, -1, 0\n\tv_mbcnt_hi_u32_b32 %0, -1, %0" : "=v"(l)); return l; }
; __device__ __forceinline__ unsigned cvt_pk_bf16(float lo, float hi) { unsigned r; asm volatile("v_cvt_pk_bf16_f32 %0, %1, %2" : "=v"(r) : "v"(lo), "v"(hi)); return r; }
;     __device__ __forceinline__ void operator()(const f32x4 (&acc)[2][2][4][2], const Unit& u, int wr, int wc, int fr_, int fq_) const {
;         const int l_ = fresh_lane(), fr = l_ & 15, fq = l_ >> 4;
;         const int row0 = u.pm * BM + wr * 64 + fr, col0 = u.pn * BM + wc * 32 + 4 * fq;
; #pragma unroll
;         for (int ai = 0; ai < 2; ++ai)
; #pragma unroll
;             for (int m = 0; m < 4; ++m) { const size_t r = (size_t)(row0 + ai * HALF + m * 16); float ss = 0.f;
; #pragma unroll
;                 for (int bj = 0; bj < 2; ++bj)
; #pragma unroll
;                     for (int n = 0; n < 2; ++n) { const size_t o = r * ldc + col0 + bj * HALF + n * 16; const f32x4 c = *(const f32x4*)(R + o) + acc[ai][bj][m][n];
;                         ss += (c[0] * c[0] + c[1] * c[1]) + (c[2] * c[2] + c[3] * c[3]);
;                         u32x2 w; w.x = cvt_pk_bf16(c[0], c[1]); w.y = cvt_pk_bf16(c[2], c[3]); *(u32x2*)(HB + o) = w; }
;                 ss += __builtin_bit_cast(float, __builtin_amdgcn_ds_bpermute((l_ ^ 16) << 2, __builtin_bit_cast(int, ss)));
;                 ss += __builtin_bit_cast(float, __builtin_amdgcn_ds_bpermute((l_ ^ 32) << 2, __builtin_bit_cast(int, ss)));
;                 if (fq == 0) PSQ[r * 64 + u.pn * 4 + wc] = ss;
.LBB0_3067:
	s_lshl_b32 s41, s48, 8
	s_add_i32 s41, s41, s67
	v_mbcnt_lo_u32_b32 v158, -1, 0
	v_mbcnt_hi_u32_b32 v158, -1, v158
	s_lshl_b32 s48, s12, 2
	v_and_or_b32 v140, v158, 15, s41
	s_lshl_b32 s41, s12, 8
	v_ashrrev_i32_e32 v134, 2, v158
	s_or_b32 s41, s41, s70
	v_and_b32_e32 v134, -4, v134
	v_add_u32_e32 v138, s41, v134
	v_ashrrev_i32_e32 v141, 31, v140
	v_ashrrev_i32_e32 v139, 31, v138
	v_lshlrev_b64 v[134:135], 12, v[140:141]
	v_lshl_add_u64 v[136:137], v[134:135], 0, v[138:139]
	v_lshl_add_u64 v[150:151], v[136:137], 2, s[36:37]
	v_mov_b32_e32 v240, v140
	v_ashrrev_i32_e32 v241, 31, v240
	v_lshlrev_b64 v[240:241], 12, v[240:241]
	v_lshl_add_u64 v[240:241], v[240:241], 0, v[138:139]
	v_lshl_add_u64 v[240:241], v[240:241], 2, s[36:37]
	global_load_dwordx4 v[160:163], v[240:241], off nt
	global_load_dwordx4 v[164:167], v[240:241], off offset:64 nt
	global_load_dwordx4 v[168:171], v[240:241], off offset:512 nt
	global_load_dwordx4 v[172:175], v[240:241], off offset:576 nt
	v_or_b32_e32 v240, 16, v140
	v_ashrrev_i32_e32 v241, 31, v240
	v_lshlrev_b64 v[240:241], 12, v[240:241]
	v_lshl_add_u64 v[240:241], v[240:241], 0, v[138:139]
	v_lshl_add_u64 v[240:241], v[240:241], 2, s[36:37]
	global_load_dwordx4 v[176:179], v[240:241], off nt
	global_load_dwordx4 v[180:183], v[240:241], off offset:64 nt
	global_load_dwordx4 v[184:187], v[240:241], off offset:512 nt
	global_load_dwordx4 v[188:191], v[240:241], off offset:576 nt
	v_or_b32_e32 v240, 32, v140
	v_ashrrev_i32_e32 v241, 31, v240
	v_lshlrev_b64 v[240:241], 12, v[240:241]
	v_lshl_add_u64 v[240:241], v[240:241], 0, v[138:139]
	v_lshl_add_u64 v[240:241], v[240:241], 2, s[36:37]
	global_load_dwordx4 v[192:195], v[240:241], off nt
	global_load_dwordx4 v[196:199], v[240:241], off offset:64 nt
	global_load_dwordx4 v[200:203], v[240:241], off offset:512 nt
	global_load_dwordx4 v[204:207], v[240:241], off offset:576 nt
	v_or_b32_e32 v240, 48, v140
	v_ashrrev_i32_e32 v241, 31, v240
	v_lshlrev_b64 v[240:241], 12, v[240:241]
	v_lshl_add_u64 v[240:241], v[240:241], 0, v[138:139]
	v_lshl_add_u64 v[240:241], v[240:241], 2, s[36:37]
	global_load_dwordx4 v[208:211], v[240:241], off nt
	global_load_dwordx4 v[212:215], v[240:241], off offset:64 nt
	global_load_dwordx4 v[216:219], v[240:241], off offset:512 nt
	global_load_dwordx4 v[220:223], v[240:241], off offset:576 nt
	v_or_b32_e32 v240, 128, v140
	v_ashrrev_i32_e32 v241, 31, v240
	v_lshlrev_b64 v[240:241], 12, v[240:241]
	v_lshl_add_u64 v[240:241], v[240:241], 0, v[138:139]
	v_lshl_add_u64 v[240:241], v[240:241], 2, s[36:37]
	global_load_dwordx4 v[224:227], v[240:241], off nt
	global_load_dwordx4 v[228:231], v[240:241], off offset:64 nt
	global_load_dwordx4 v[232:235], v[240:241], off offset:512 nt
	global_load_dwordx4 v[236:239], v[240:241], off offset:576 nt
	s_waitcnt vmcnt(19)
	v_mov_b64_e32 v[146:147], v[160:161]
	v_mov_b64_e32 v[148:149], v[162:163]
	v_lshl_add_u64 v[136:137], v[136:137], 1, s[14:15]
	v_cmp_gt_u32_e32 vcc, 16, v158
	s_ashr_i32 s49, s48, 31
	v_pk_add_f32 v[128:129], v[128:129], v[148:149]
	v_pk_add_f32 v[152:153], v[126:127], v[146:147]
	s_nop 0
	v_cvt_pk_bf16_f32 v126, v152, v153
	v_cvt_pk_bf16_f32 v127, v128, v129
	global_store_dwordx2 v[136:137], v[126:127], off
	s_waitcnt vmcnt(19)
	v_mov_b64_e32 v[146:147], v[164:165]
	v_mov_b64_e32 v[148:149], v[166:167]
	v_lshl_add_u64 v[126:127], v[138:139], 0, 16
	v_lshl_add_u64 v[136:137], v[126:127], 0, v[134:135]
	v_lshl_add_u64 v[136:137], v[136:137], 1, s[14:15]
	v_mul_f32_e32 v129, v129, v129
	v_fmac_f32_e32 v129, v128, v128
	v_pk_add_f32 v[124:125], v[124:125], v[148:149]
	v_pk_add_f32 v[154:155], v[122:123], v[146:147]
	s_nop 0
	v_cvt_pk_bf16_f32 v122, v154, v155
	v_cvt_pk_bf16_f32 v123, v124, v125
	global_store_dwordx2 v[136:137], v[122:123], off
	s_waitcnt vmcnt(19)
	v_mov_b64_e32 v[146:147], v[168:169]
	v_mov_b64_e32 v[148:149], v[170:171]
	v_lshl_add_u64 v[122:123], v[138:139], 0, s[18:19]
	v_lshl_add_u64 v[136:137], v[122:123], 0, v[134:135]
	v_lshl_add_u64 v[136:137], v[136:137], 1, s[14:15]
	v_mul_f32_e32 v125, v125, v125
	v_fmac_f32_e32 v125, v124, v124
	v_pk_add_f32 v[120:121], v[120:121], v[148:149]
	v_pk_add_f32 v[156:157], v[118:119], v[146:147]
	s_nop 0
	v_cvt_pk_bf16_f32 v118, v156, v157
	v_cvt_pk_bf16_f32 v119, v120, v121
	global_store_dwordx2 v[136:137], v[118:119], off
	s_waitcnt vmcnt(19)
	v_mov_b64_e32 v[146:147], v[172:173]
	v_mov_b64_e32 v[148:149], v[174:175]
	v_or_b32_e32 v240, 144, v140
	v_ashrrev_i32_e32 v241, 31, v240
	v_lshlrev_b64 v[240:241], 12, v[240:241]
	v_lshl_add_u64 v[240:241], v[240:241], 0, v[138:139]
	v_lshl_add_u64 v[240:241], v[240:241], 2, s[36:37]
	global_load_dwordx4 v[160:163], v[240:241], off nt
	global_load_dwordx4 v[164:167], v[240:241], off offset:64 nt
	global_load_dwordx4 v[168:171], v[240:241], off offset:512 nt
	global_load_dwordx4 v[172:175], v[240:241], off offset:576 nt
	v_mul_f32_e32 v136, v153, v153
	v_fmac_f32_e32 v136, v152, v152
	v_add_f32_e32 v128, v136, v129
	v_mul_f32_e32 v129, v155, v155
	v_fmac_f32_e32 v129, v154, v154
	v_add_f32_e32 v124, v129, v125
	v_mul_f32_e32 v125, v157, v157
	v_mul_f32_e32 v121, v121, v121
	v_fmac_f32_e32 v125, v156, v156
	v_fmac_f32_e32 v121, v120, v120
	v_add_f32_e32 v124, v128, v124
	v_add_f32_e32 v120, v125, v121
	v_add_f32_e32 v128, v124, v120
	v_lshlrev_b32_e32 v118, 2, v158
	v_xor_b32_e32 v119, 64, v118
	v_xor_b32_e32 v118, 0x80, v118
	v_pk_add_f32 v[120:121], v[116:117], v[148:149]
	v_pk_add_f32 v[124:125], v[114:115], v[146:147]
	v_mul_f32_e32 v115, v121, v121
	v_mul_f32_e32 v114, v125, v125
	v_fmac_f32_e32 v114, v124, v124
	v_fmac_f32_e32 v115, v120, v120
	v_add_f32_e32 v114, v114, v115
	v_add_f32_e32 v116, v128, v114
	ds_bpermute_b32 v117, v119, v116
	v_lshl_add_u64 v[114:115], v[138:139], 0, s[38:39]
	v_lshl_add_u64 v[128:129], v[114:115], 0, v[134:135]
	v_cvt_pk_bf16_f32 v124, v124, v125
	v_cvt_pk_bf16_f32 v125, v120, v121
	s_waitcnt lgkmcnt(0)
	v_add_f32_e32 v116, v116, v117
	ds_bpermute_b32 v117, v118, v116
	v_lshl_add_u64 v[120:121], v[128:129], 1, s[14:15]
	global_store_dwordx2 v[120:121], v[124:125], off
	s_and_saveexec_b64 s[50:51], vcc
	s_cbranch_execz .LBB0_3069
	v_lshlrev_b64 v[120:121], 8, v[140:141]
	v_lshl_add_u64 v[120:121], s[16:17], 0, v[120:121]
	v_lshl_add_u64 v[120:121], s[48:49], 2, v[120:121]
	s_lshl_b32 s12, s66, 2
	v_lshl_add_u64 v[120:121], v[120:121], 0, s[12:13]
	s_waitcnt lgkmcnt(0)
	v_add_f32_e32 v116, v116, v117
	global_store_dword v[120:121], v116, off
; __device__ __forceinline__ int fresh_lane() { int l; asm volatile("v_mbcnt_lo_u32_b32 %0, -1, 0\n\tv_mbcnt_hi_u32_b32 %0, -1, %0" : "=v"(l)); return l; }
; __device__ __forceinline__ unsigned cvt_pk_bf16(float lo, float hi) { unsigned r; asm volatile("v_cvt_pk_bf16_f32 %0, %1, %2" : "=v"(r) : "v"(lo), "v"(hi)); return r; }
;     __device__ __forceinline__ void operator()(const f32x4 (&acc)[2][2][4][2], const Unit& u, int wr, int wc, int fr_, int fq_) const {
;         const int l_ = fresh_lane(), fr = l_ & 15, fq = l_ >> 4;
;         const int row0 = u.pm * BM + wr * 64 + fr, col0 = u.pn * BM + wc * 32 + 4 * fq;
; #pragma unroll
;         for (int ai = 0; ai < 2; ++ai)
; #pragma unroll
;             for (int m = 0; m < 4; ++m) { const size_t r = (size_t)(row0 + ai * HALF + m * 16); float ss = 0.f;
; #pragma unroll
;                 for (int bj = 0; bj < 2; ++bj)
; #pragma unroll
;                     for (int n = 0; n < 2; ++n) { const size_t o = r * ldc + col0 + bj * HALF + n * 16; const f32x4 c = *(const f32x4*)(R + o) + acc[ai][bj][m][n];
;                         ss += (c[0] * c[0] + c[1] * c[1]) + (c[2] * c[2] + c[3] * c[3]);
;                         u32x2 w; w.x = cvt_pk_bf16(c[0], c[1]); w.y = cvt_pk_bf16(c[2], c[3]); *(u32x2*)(HB + o) = w; }
;                 ss += __builtin_bit_cast(float, __builtin_amdgcn_ds_bpermute((l_ ^ 16) << 2, __builtin_bit_cast(int, ss)));
;                 ss += __builtin_bit_cast(float, __builtin_amdgcn_ds_bpermute((l_ ^ 32) << 2, __builtin_bit_cast(int, ss)));
;                 if (fq == 0) PSQ[r * 64 + u.pn * 4 + wc] = ss;
.LBB0_3069:
	s_or_b64 exec, exec, s[50:51]
	v_or_b32_e32 v116, 16, v140
	s_waitcnt lgkmcnt(0)
	v_ashrrev_i32_e32 v117, 31, v116
	v_lshlrev_b64 v[120:121], 12, v[116:117]
	v_lshl_add_u64 v[124:125], v[120:121], 0, v[138:139]
	v_lshl_add_u64 v[128:129], v[124:125], 2, s[36:37]
	s_waitcnt vmcnt(24)
	v_mov_b64_e32 v[146:147], v[176:177]
	v_mov_b64_e32 v[148:149], v[178:179]
	v_lshl_add_u64 v[124:125], v[124:125], 1, s[14:15]
	v_pk_add_f32 v[134:135], v[112:113], v[148:149]
	v_pk_add_f32 v[136:137], v[110:111], v[146:147]
	s_nop 0
	v_cvt_pk_bf16_f32 v110, v136, v137
	v_cvt_pk_bf16_f32 v111, v134, v135
	global_store_dwordx2 v[124:125], v[110:111], off
	s_waitcnt vmcnt(24)
	v_mov_b64_e32 v[110:111], v[180:181]
	v_mov_b64_e32 v[112:113], v[182:183]
	v_lshl_add_u64 v[124:125], v[120:121], 0, v[126:127]
	v_lshl_add_u64 v[124:125], v[124:125], 1, s[14:15]
	v_pk_add_f32 v[112:113], v[108:109], v[112:113]
	v_pk_add_f32 v[110:111], v[106:107], v[110:111]
	s_nop 0
	v_cvt_pk_bf16_f32 v106, v110, v111
	v_cvt_pk_bf16_f32 v107, v112, v113
	global_store_dwordx2 v[124:125], v[106:107], off
	s_waitcnt vmcnt(24)
	v_mov_b64_e32 v[106:107], v[184:185]
	v_mov_b64_e32 v[108:109], v[186:187]
	v_lshl_add_u64 v[124:125], v[120:121], 0, v[122:123]
	v_lshl_add_u64 v[124:125], v[124:125], 1, s[14:15]
	v_mul_f32_e32 v111, v111, v111
	v_mul_f32_e32 v113, v113, v113
	v_fmac_f32_e32 v111, v110, v110
	v_fmac_f32_e32 v113, v112, v112
	v_add_f32_e32 v110, v111, v113
	v_pk_add_f32 v[108:109], v[104:105], v[108:109]
	v_pk_add_f32 v[106:107], v[102:103], v[106:107]
	s_nop 0
	v_cvt_pk_bf16_f32 v102, v106, v107
	v_cvt_pk_bf16_f32 v103, v108, v109
	global_store_dwordx2 v[124:125], v[102:103], off
	s_waitcnt vmcnt(24)
	v_mov_b64_e32 v[102:103], v[188:189]
	v_mov_b64_e32 v[104:105], v[190:191]
	v_or_b32_e32 v240, 160, v140
	v_ashrrev_i32_e32 v241, 31, v240
	v_lshlrev_b64 v[240:241], 12, v[240:241]
	v_lshl_add_u64 v[240:241], v[240:241], 0, v[138:139]
	v_lshl_add_u64 v[240:241], v[240:241], 2, s[36:37]
	global_load_dwordx4 v[176:179], v[240:241], off nt
	global_load_dwordx4 v[180:183], v[240:241], off offset:64 nt
	global_load_dwordx4 v[184:187], v[240:241], off offset:512 nt
	global_load_dwordx4 v[188:191], v[240:241], off offset:576 nt
	v_mul_f32_e32 v124, v137, v137
	v_mul_f32_e32 v125, v135, v135
	v_fmac_f32_e32 v124, v136, v136
	v_fmac_f32_e32 v125, v134, v134
	v_mul_f32_e32 v107, v107, v107
	v_mul_f32_e32 v109, v109, v109
	v_add_f32_e32 v124, v124, v125
	v_fmac_f32_e32 v107, v106, v106
	v_fmac_f32_e32 v109, v108, v108
	v_add_f32_e32 v110, v124, v110
	v_add_f32_e32 v106, v107, v109
	v_add_f32_e32 v106, v110, v106
	v_pk_add_f32 v[100:101], v[100:101], v[104:105]
	v_pk_add_f32 v[102:103], v[98:99], v[102:103]
	v_mul_f32_e32 v99, v101, v101
	v_mul_f32_e32 v98, v103, v103
	v_fmac_f32_e32 v98, v102, v102
	v_fmac_f32_e32 v99, v100, v100
	v_add_f32_e32 v98, v98, v99
	v_add_f32_e32 v98, v106, v98
	ds_bpermute_b32 v99, v119, v98
	v_lshl_add_u64 v[104:105], v[120:121], 0, v[114:115]
	v_cvt_pk_bf16_f32 v102, v102, v103
	v_cvt_pk_bf16_f32 v103, v100, v101
	v_lshl_add_u64 v[100:101], v[104:105], 1, s[14:15]
	s_waitcnt lgkmcnt(0)
	v_add_f32_e32 v98, v98, v99
	ds_bpermute_b32 v99, v118, v98
	global_store_dwordx2 v[100:101], v[102:103], off
	s_and_saveexec_b64 s[50:51], vcc
	s_cbranch_execz .LBB0_3071
	v_lshlrev_b64 v[100:101], 8, v[116:117]
	v_lshl_add_u64 v[100:101], s[16:17], 0, v[100:101]
	v_lshl_add_u64 v[100:101], s[48:49], 2, v[100:101]
	s_lshl_b32 s12, s66, 2
	v_lshl_add_u64 v[100:101], v[100:101], 0, s[12:13]
	s_waitcnt lgkmcnt(0)
	v_add_f32_e32 v98, v98, v99
	global_store_dword v[100:101], v98, off
.LBB0_3071:
	s_or_b64 exec, exec, s[50:51]
	v_or_b32_e32 v98, 32, v140
	s_waitcnt lgkmcnt(0)
	v_ashrrev_i32_e32 v99, 31, v98
	v_lshlrev_b64 v[104:105], 12, v[98:99]
	v_lshl_add_u64 v[106:107], v[104:105], 0, v[138:139]
	v_lshl_add_u64 v[108:109], v[106:107], 2, s[36:37]
	s_waitcnt vmcnt(29)
	v_mov_b64_e32 v[100:101], v[192:193]
	v_mov_b64_e32 v[102:103], v[194:195]
	v_lshl_add_u64 v[106:107], v[106:107], 1, s[14:15]
	v_pk_add_f32 v[102:103], v[96:97], v[102:103]
	v_pk_add_f32 v[100:101], v[94:95], v[100:101]
	s_nop 0
	v_cvt_pk_bf16_f32 v94, v100, v101
	v_cvt_pk_bf16_f32 v95, v102, v103
	global_store_dwordx2 v[106:107], v[94:95], off
	s_waitcnt vmcnt(29)
	v_mov_b64_e32 v[94:95], v[196:197]
	v_mov_b64_e32 v[96:97], v[198:199]
	v_lshl_add_u64 v[106:107], v[104:105], 0, v[126:127]
	v_lshl_add_u64 v[106:107], v[106:107], 1, s[14:15]
	v_mul_f32_e32 v101, v101, v101
	v_mul_f32_e32 v103, v103, v103
	v_fmac_f32_e32 v101, v100, v100
	v_fmac_f32_e32 v103, v102, v102
	v_add_f32_e32 v100, v101, v103
	v_pk_add_f32 v[96:97], v[92:93], v[96:97]
	v_pk_add_f32 v[94:95], v[90:91], v[94:95]
	s_nop 0
	v_cvt_pk_bf16_f32 v90, v94, v95
	v_cvt_pk_bf16_f32 v91, v96, v97
	global_store_dwordx2 v[106:107], v[90:91], off
	s_waitcnt vmcnt(29)
	v_mov_b64_e32 v[90:91], v[200:201]
	v_mov_b64_e32 v[92:93], v[202:203]
	v_lshl_add_u64 v[106:107], v[104:105], 0, v[122:123]
	v_lshl_add_u64 v[106:107], v[106:107], 1, s[14:15]
	v_mul_f32_e32 v95, v95, v95
	v_mul_f32_e32 v97, v97, v97
	v_fmac_f32_e32 v95, v94, v94
	v_fmac_f32_e32 v97, v96, v96
	v_add_f32_e32 v94, v95, v97
	v_add_f32_e32 v94, v100, v94
	v_pk_add_f32 v[92:93], v[88:89], v[92:93]
	v_pk_add_f32 v[90:91], v[86:87], v[90:91]
	s_nop 0
	v_cvt_pk_bf16_f32 v86, v90, v91
	v_cvt_pk_bf16_f32 v87, v92, v93
	global_store_dwordx2 v[106:107], v[86:87], off
	s_waitcnt vmcnt(29)
	v_mov_b64_e32 v[86:87], v[204:205]
	v_mov_b64_e32 v[88:89], v[206:207]
	v_or_b32_e32 v240, 176, v140
	v_ashrrev_i32_e32 v241, 31, v240
	v_lshlrev_b64 v[240:241], 12, v[240:241]
	v_lshl_add_u64 v[240:241], v[240:241], 0, v[138:139]
	v_lshl_add_u64 v[240:241], v[240:241], 2, s[36:37]
	global_load_dwordx4 v[192:195], v[240:241], off nt
	global_load_dwordx4 v[196:199], v[240:241], off offset:64 nt
	global_load_dwordx4 v[200:203], v[240:241], off offset:512 nt
	global_load_dwordx4 v[204:207], v[240:241], off offset:576 nt
	v_mul_f32_e32 v91, v91, v91
	v_mul_f32_e32 v93, v93, v93
	v_fmac_f32_e32 v91, v90, v90
	v_fmac_f32_e32 v93, v92, v92
	v_add_f32_e32 v90, v91, v93
	v_add_f32_e32 v90, v94, v90
	v_pk_add_f32 v[84:85], v[84:85], v[88:89]
	v_pk_add_f32 v[86:87], v[82:83], v[86:87]
	v_mul_f32_e32 v83, v85, v85
	v_mul_f32_e32 v82, v87, v87
	v_fmac_f32_e32 v82, v86, v86
	v_fmac_f32_e32 v83, v84, v84
	v_add_f32_e32 v82, v82, v83
	v_add_f32_e32 v82, v90, v82
	ds_bpermute_b32 v83, v119, v82
	v_lshl_add_u64 v[88:89], v[104:105], 0, v[114:115]
	v_cvt_pk_bf16_f32 v86, v86, v87
	v_cvt_pk_bf16_f32 v87, v84, v85
	v_lshl_add_u64 v[84:85], v[88:89], 1, s[14:15]
	s_waitcnt lgkmcnt(0)
	v_add_f32_e32 v82, v82, v83
	ds_bpermute_b32 v83, v118, v82
	global_store_dwordx2 v[84:85], v[86:87], off
	s_and_saveexec_b64 s[50:51], vcc
	s_cbranch_execz .LBB0_3073
; __device__ __forceinline__ int fresh_lane() { int l; asm volatile("v_mbcnt_lo_u32_b32 %0, -1, 0\n\tv_mbcnt_hi_u32_b32 %0, -1, %0" : "=v"(l)); return l; }
; __device__ __forceinline__ unsigned cvt_pk_bf16(float lo, float hi) { unsigned r; asm volatile("v_cvt_pk_bf16_f32 %0, %1, %2" : "=v"(r) : "v"(lo), "v"(hi)); return r; }
;     __device__ __forceinline__ void operator()(const f32x4 (&acc)[2][2][4][2], const Unit& u, int wr, int wc, int fr_, int fq_) const {
;         const int l_ = fresh_lane(), fr = l_ & 15, fq = l_ >> 4;
;         const int row0 = u.pm * BM + wr * 64 + fr, col0 = u.pn * BM + wc * 32 + 4 * fq;
; #pragma unroll
;         for (int ai = 0; ai < 2; ++ai)
; #pragma unroll
;             for (int m = 0; m < 4; ++m) { const size_t r = (size_t)(row0 + ai * HALF + m * 16); float ss = 0.f;
; #pragma unroll
;                 for (int bj = 0; bj < 2; ++bj)
; #pragma unroll
;                     for (int n = 0; n < 2; ++n) { const size_t o = r * ldc + col0 + bj * HALF + n * 16; const f32x4 c = *(const f32x4*)(R + o) + acc[ai][bj][m][n];
;                         ss += (c[0] * c[0] + c[1] * c[1]) + (c[2] * c[2] + c[3] * c[3]);
;                         u32x2 w; w.x = cvt_pk_bf16(c[0], c[1]); w.y = cvt_pk_bf16(c[2], c[3]); *(u32x2*)(HB + o) = w; }
;                 ss += __builtin_bit_cast(float, __builtin_amdgcn_ds_bpermute((l_ ^ 16) << 2, __builtin_bit_cast(int, ss)));
;                 ss += __builtin_bit_cast(float, __builtin_amdgcn_ds_bpermute((l_ ^ 32) << 2, __builtin_bit_cast(int, ss)));
;                 if (fq == 0) PSQ[r * 64 + u.pn * 4 + wc] = ss;
	v_lshlrev_b64 v[84:85], 8, v[98:99]
	v_lshl_add_u64 v[84:85], s[16:17], 0, v[84:85]
	v_lshl_add_u64 v[84:85], s[48:49], 2, v[84:85]
	s_lshl_b32 s12, s66, 2
	v_lshl_add_u64 v[84:85], v[84:85], 0, s[12:13]
	s_waitcnt lgkmcnt(0)
	v_add_f32_e32 v82, v82, v83
	global_store_dword v[84:85], v82, off
.LBB0_3073:
	s_or_b64 exec, exec, s[50:51]
	v_or_b32_e32 v82, 48, v140
	s_waitcnt lgkmcnt(0)
	v_ashrrev_i32_e32 v83, 31, v82
	v_lshlrev_b64 v[88:89], 12, v[82:83]
	v_lshl_add_u64 v[90:91], v[88:89], 0, v[138:139]
	v_lshl_add_u64 v[92:93], v[90:91], 2, s[36:37]
	s_waitcnt vmcnt(34)
	v_mov_b64_e32 v[84:85], v[208:209]
	v_mov_b64_e32 v[86:87], v[210:211]
	v_lshl_add_u64 v[90:91], v[90:91], 1, s[14:15]
	v_pk_add_f32 v[86:87], v[80:81], v[86:87]
	v_pk_add_f32 v[84:85], v[78:79], v[84:85]
	s_nop 0
	v_cvt_pk_bf16_f32 v78, v84, v85
	v_cvt_pk_bf16_f32 v79, v86, v87
	global_store_dwordx2 v[90:91], v[78:79], off
	s_waitcnt vmcnt(34)
	v_mov_b64_e32 v[78:79], v[212:213]
	v_mov_b64_e32 v[80:81], v[214:215]
	v_lshl_add_u64 v[90:91], v[88:89], 0, v[126:127]
	v_lshl_add_u64 v[90:91], v[90:91], 1, s[14:15]
	v_mul_f32_e32 v85, v85, v85
	v_mul_f32_e32 v87, v87, v87
	v_fmac_f32_e32 v85, v84, v84
	v_fmac_f32_e32 v87, v86, v86
	v_add_f32_e32 v84, v85, v87
	v_pk_add_f32 v[80:81], v[76:77], v[80:81]
	v_pk_add_f32 v[78:79], v[74:75], v[78:79]
	s_nop 0
	v_cvt_pk_bf16_f32 v74, v78, v79
	v_cvt_pk_bf16_f32 v75, v80, v81
	global_store_dwordx2 v[90:91], v[74:75], off
	s_waitcnt vmcnt(34)
	v_mov_b64_e32 v[74:75], v[216:217]
	v_mov_b64_e32 v[76:77], v[218:219]
	v_lshl_add_u64 v[90:91], v[88:89], 0, v[122:123]
	v_lshl_add_u64 v[90:91], v[90:91], 1, s[14:15]
	v_mul_f32_e32 v79, v79, v79
	v_mul_f32_e32 v81, v81, v81
	v_fmac_f32_e32 v79, v78, v78
	v_fmac_f32_e32 v81, v80, v80
	v_add_f32_e32 v78, v79, v81
	v_add_f32_e32 v78, v84, v78
	v_pk_add_f32 v[76:77], v[72:73], v[76:77]
	v_pk_add_f32 v[74:75], v[70:71], v[74:75]
	s_nop 0
	v_cvt_pk_bf16_f32 v70, v74, v75
	v_cvt_pk_bf16_f32 v71, v76, v77
	global_store_dwordx2 v[90:91], v[70:71], off
	s_waitcnt vmcnt(34)
	v_mov_b64_e32 v[70:71], v[220:221]
	v_mov_b64_e32 v[72:73], v[222:223]
	v_mul_f32_e32 v75, v75, v75
	v_mul_f32_e32 v77, v77, v77
	v_fmac_f32_e32 v75, v74, v74
	v_fmac_f32_e32 v77, v76, v76
	v_add_f32_e32 v74, v75, v77
	v_add_f32_e32 v74, v78, v74
	v_pk_add_f32 v[68:69], v[68:69], v[72:73]
	v_pk_add_f32 v[70:71], v[66:67], v[70:71]
	v_mul_f32_e32 v67, v69, v69
	v_mul_f32_e32 v66, v71, v71
	v_fmac_f32_e32 v66, v70, v70
	v_fmac_f32_e32 v67, v68, v68
	v_add_f32_e32 v66, v66, v67
	v_add_f32_e32 v66, v74, v66
	ds_bpermute_b32 v67, v119, v66
	v_lshl_add_u64 v[72:73], v[88:89], 0, v[114:115]
	v_cvt_pk_bf16_f32 v70, v70, v71
	v_cvt_pk_bf16_f32 v71, v68, v69
	v_lshl_add_u64 v[68:69], v[72:73], 1, s[14:15]
	s_waitcnt lgkmcnt(0)
	v_add_f32_e32 v66, v66, v67
	ds_bpermute_b32 v67, v118, v66
	global_store_dwordx2 v[68:69], v[70:71], off
	s_and_saveexec_b64 s[50:51], vcc
	s_cbranch_execz .LBB0_3075
	v_lshlrev_b64 v[68:69], 8, v[82:83]
	v_lshl_add_u64 v[68:69], s[16:17], 0, v[68:69]
	v_lshl_add_u64 v[68:69], s[48:49], 2, v[68:69]
	s_lshl_b32 s12, s66, 2
	v_lshl_add_u64 v[68:69], v[68:69], 0, s[12:13]
	s_waitcnt lgkmcnt(0)
	v_add_f32_e32 v66, v66, v67
	global_store_dword v[68:69], v66, off
.LBB0_3075:
	s_or_b64 exec, exec, s[50:51]
	v_add_u32_e32 v66, 0x80, v140
	s_waitcnt lgkmcnt(0)
	v_ashrrev_i32_e32 v67, 31, v66
	v_lshlrev_b64 v[72:73], 12, v[66:67]
	v_lshl_add_u64 v[74:75], v[72:73], 0, v[138:139]
	v_lshl_add_u64 v[76:77], v[74:75], 2, s[36:37]
	s_waitcnt vmcnt(35)
	v_mov_b64_e32 v[68:69], v[224:225]
	v_mov_b64_e32 v[70:71], v[226:227]
	v_lshl_add_u64 v[74:75], v[74:75], 1, s[14:15]
	v_pk_add_f32 v[70:71], v[64:65], v[70:71]
	v_pk_add_f32 v[68:69], v[62:63], v[68:69]
	s_nop 0
	v_cvt_pk_bf16_f32 v62, v68, v69
	v_cvt_pk_bf16_f32 v63, v70, v71
	global_store_dwordx2 v[74:75], v[62:63], off
	s_waitcnt vmcnt(35)
	v_mov_b64_e32 v[62:63], v[228:229]
	v_mov_b64_e32 v[64:65], v[230:231]
	v_lshl_add_u64 v[74:75], v[72:73], 0, v[126:127]
	v_lshl_add_u64 v[74:75], v[74:75], 1, s[14:15]
	v_mul_f32_e32 v69, v69, v69
	v_mul_f32_e32 v71, v71, v71
	v_fmac_f32_e32 v69, v68, v68
	v_fmac_f32_e32 v71, v70, v70
	v_add_f32_e32 v68, v69, v71
	v_pk_add_f32 v[64:65], v[60:61], v[64:65]
	v_pk_add_f32 v[62:63], v[58:59], v[62:63]
	s_nop 0
	v_cvt_pk_bf16_f32 v58, v62, v63
	v_cvt_pk_bf16_f32 v59, v64, v65
	global_store_dwordx2 v[74:75], v[58:59], off
	s_waitcnt vmcnt(35)
	v_mov_b64_e32 v[58:59], v[232:233]
	v_mov_b64_e32 v[60:61], v[234:235]
	v_lshl_add_u64 v[74:75], v[72:73], 0, v[122:123]
	v_lshl_add_u64 v[74:75], v[74:75], 1, s[14:15]
	v_mul_f32_e32 v63, v63, v63
	v_mul_f32_e32 v65, v65, v65
	v_fmac_f32_e32 v63, v62, v62
	v_fmac_f32_e32 v65, v64, v64
	v_add_f32_e32 v62, v63, v65
	v_add_f32_e32 v62, v68, v62
	v_pk_add_f32 v[60:61], v[56:57], v[60:61]
	v_pk_add_f32 v[58:59], v[54:55], v[58:59]
	s_nop 0
	v_cvt_pk_bf16_f32 v54, v58, v59
	v_cvt_pk_bf16_f32 v55, v60, v61
	global_store_dwordx2 v[74:75], v[54:55], off
	s_waitcnt vmcnt(35)
	v_mov_b64_e32 v[54:55], v[236:237]
	v_mov_b64_e32 v[56:57], v[238:239]
	v_mul_f32_e32 v59, v59, v59
	v_mul_f32_e32 v61, v61, v61
	v_fmac_f32_e32 v59, v58, v58
	v_fmac_f32_e32 v61, v60, v60
	v_add_f32_e32 v58, v59, v61
	v_add_f32_e32 v58, v62, v58
	v_pk_add_f32 v[52:53], v[52:53], v[56:57]
	v_pk_add_f32 v[54:55], v[50:51], v[54:55]
	v_mul_f32_e32 v51, v53, v53
	v_mul_f32_e32 v50, v55, v55
	v_fmac_f32_e32 v50, v54, v54
	v_fmac_f32_e32 v51, v52, v52
	v_add_f32_e32 v50, v50, v51
	v_add_f32_e32 v50, v58, v50
	ds_bpermute_b32 v51, v119, v50
	v_lshl_add_u64 v[56:57], v[72:73], 0, v[114:115]
	v_cvt_pk_bf16_f32 v54, v54, v55
	v_cvt_pk_bf16_f32 v55, v52, v53
	v_lshl_add_u64 v[52:53], v[56:57], 1, s[14:15]
	s_waitcnt lgkmcnt(0)
	v_add_f32_e32 v50, v50, v51
	ds_bpermute_b32 v51, v118, v50
	global_store_dwordx2 v[52:53], v[54:55], off
	s_and_saveexec_b64 s[50:51], vcc
	s_cbranch_execz .LBB0_3077
	v_lshlrev_b64 v[52:53], 8, v[66:67]
	v_lshl_add_u64 v[52:53], s[16:17], 0, v[52:53]
	v_lshl_add_u64 v[52:53], s[48:49], 2, v[52:53]
	s_lshl_b32 s12, s66, 2
	v_lshl_add_u64 v[52:53], v[52:53], 0, s[12:13]
	s_waitcnt lgkmcnt(0)
	v_add_f32_e32 v50, v50, v51
	global_store_dword v[52:53], v50, off
; __device__ __forceinline__ int fresh_lane() { int l; asm volatile("v_mbcnt_lo_u32_b32 %0, -1, 0\n\tv_mbcnt_hi_u32_b32 %0, -1, %0" : "=v"(l)); return l; }
; __device__ __forceinline__ unsigned cvt_pk_bf16(float lo, float hi) { unsigned r; asm volatile("v_cvt_pk_bf16_f32 %0, %1, %2" : "=v"(r) : "v"(lo), "v"(hi)); return r; }
;     __device__ __forceinline__ void operator()(const f32x4 (&acc)[2][2][4][2], const Unit& u, int wr, int wc, int fr_, int fq_) const {
;         const int l_ = fresh_lane(), fr = l_ & 15, fq = l_ >> 4;
;         const int row0 = u.pm * BM + wr * 64 + fr, col0 = u.pn * BM + wc * 32 + 4 * fq;
; #pragma unroll
;         for (int ai = 0; ai < 2; ++ai)
; #pragma unroll
;             for (int m = 0; m < 4; ++m) { const size_t r = (size_t)(row0 + ai * HALF + m * 16); float ss = 0.f;
; #pragma unroll
;                 for (int bj = 0; bj < 2; ++bj)
; #pragma unroll
;                     for (int n = 0; n < 2; ++n) { const size_t o = r * ldc + col0 + bj * HALF + n * 16; const f32x4 c = *(const f32x4*)(R + o) + acc[ai][bj][m][n];
;                         ss += (c[0] * c[0] + c[1] * c[1]) + (c[2] * c[2] + c[3] * c[3]);
;                         u32x2 w; w.x = cvt_pk_bf16(c[0], c[1]); w.y = cvt_pk_bf16(c[2], c[3]); *(u32x2*)(HB + o) = w; }
;                 ss += __builtin_bit_cast(float, __builtin_amdgcn_ds_bpermute((l_ ^ 16) << 2, __builtin_bit_cast(int, ss)));
;                 ss += __builtin_bit_cast(float, __builtin_amdgcn_ds_bpermute((l_ ^ 32) << 2, __builtin_bit_cast(int, ss)));
;                 if (fq == 0) PSQ[r * 64 + u.pn * 4 + wc] = ss;
.LBB0_3077:
	s_or_b64 exec, exec, s[50:51]
	v_add_u32_e32 v50, 0x90, v140
	s_waitcnt lgkmcnt(0)
	v_ashrrev_i32_e32 v51, 31, v50
	v_lshlrev_b64 v[56:57], 12, v[50:51]
	v_lshl_add_u64 v[58:59], v[56:57], 0, v[138:139]
	v_lshl_add_u64 v[60:61], v[58:59], 2, s[36:37]
	s_waitcnt vmcnt(33)
	v_mov_b64_e32 v[52:53], v[160:161]
	v_mov_b64_e32 v[54:55], v[162:163]
	v_lshl_add_u64 v[58:59], v[58:59], 1, s[14:15]
	v_pk_add_f32 v[54:55], v[48:49], v[54:55]
	v_pk_add_f32 v[52:53], v[46:47], v[52:53]
	s_nop 0
	v_cvt_pk_bf16_f32 v46, v52, v53
	v_cvt_pk_bf16_f32 v47, v54, v55
	global_store_dwordx2 v[58:59], v[46:47], off
	s_waitcnt vmcnt(33)
	v_mov_b64_e32 v[46:47], v[164:165]
	v_mov_b64_e32 v[48:49], v[166:167]
	v_lshl_add_u64 v[58:59], v[56:57], 0, v[126:127]
	v_lshl_add_u64 v[58:59], v[58:59], 1, s[14:15]
	v_mul_f32_e32 v53, v53, v53
	v_mul_f32_e32 v55, v55, v55
	v_fmac_f32_e32 v53, v52, v52
	v_fmac_f32_e32 v55, v54, v54
	v_add_f32_e32 v52, v53, v55
	v_pk_add_f32 v[48:49], v[44:45], v[48:49]
	v_pk_add_f32 v[46:47], v[42:43], v[46:47]
	s_nop 0
	v_cvt_pk_bf16_f32 v42, v46, v47
	v_cvt_pk_bf16_f32 v43, v48, v49
	global_store_dwordx2 v[58:59], v[42:43], off
	s_waitcnt vmcnt(33)
	v_mov_b64_e32 v[42:43], v[168:169]
	v_mov_b64_e32 v[44:45], v[170:171]
	v_lshl_add_u64 v[58:59], v[56:57], 0, v[122:123]
	v_lshl_add_u64 v[58:59], v[58:59], 1, s[14:15]
	v_mul_f32_e32 v47, v47, v47
	v_mul_f32_e32 v49, v49, v49
	v_fmac_f32_e32 v47, v46, v46
	v_fmac_f32_e32 v49, v48, v48
	v_add_f32_e32 v46, v47, v49
	v_add_f32_e32 v46, v52, v46
	v_pk_add_f32 v[44:45], v[40:41], v[44:45]
	v_pk_add_f32 v[42:43], v[38:39], v[42:43]
	s_nop 0
	v_cvt_pk_bf16_f32 v38, v42, v43
	v_cvt_pk_bf16_f32 v39, v44, v45
	global_store_dwordx2 v[58:59], v[38:39], off
	s_waitcnt vmcnt(33)
	v_mov_b64_e32 v[38:39], v[172:173]
	v_mov_b64_e32 v[40:41], v[174:175]
	v_mul_f32_e32 v43, v43, v43
	v_mul_f32_e32 v45, v45, v45
	v_fmac_f32_e32 v43, v42, v42
	v_fmac_f32_e32 v45, v44, v44
	v_add_f32_e32 v42, v43, v45
	v_add_f32_e32 v42, v46, v42
	v_pk_add_f32 v[36:37], v[36:37], v[40:41]
	v_pk_add_f32 v[38:39], v[34:35], v[38:39]
	v_mul_f32_e32 v35, v37, v37
	v_mul_f32_e32 v34, v39, v39
	v_fmac_f32_e32 v34, v38, v38
	v_fmac_f32_e32 v35, v36, v36
	v_add_f32_e32 v34, v34, v35
	v_add_f32_e32 v34, v42, v34
	ds_bpermute_b32 v35, v119, v34
	v_lshl_add_u64 v[40:41], v[56:57], 0, v[114:115]
	v_cvt_pk_bf16_f32 v38, v38, v39
	v_cvt_pk_bf16_f32 v39, v36, v37
	v_lshl_add_u64 v[36:37], v[40:41], 1, s[14:15]
	s_waitcnt lgkmcnt(0)
	v_add_f32_e32 v34, v34, v35
	ds_bpermute_b32 v35, v118, v34
	global_store_dwordx2 v[36:37], v[38:39], off
	s_and_saveexec_b64 s[50:51], vcc
	s_cbranch_execz .LBB0_3079
	v_lshlrev_b64 v[36:37], 8, v[50:51]
	v_lshl_add_u64 v[36:37], s[16:17], 0, v[36:37]
	v_lshl_add_u64 v[36:37], s[48:49], 2, v[36:37]
	s_lshl_b32 s12, s66, 2
	v_lshl_add_u64 v[36:37], v[36:37], 0, s[12:13]
	s_waitcnt lgkmcnt(0)
	v_add_f32_e32 v34, v34, v35
	global_store_dword v[36:37], v34, off
; __device__ __forceinline__ int fresh_lane() { int l; asm volatile("v_mbcnt_lo_u32_b32 %0, -1, 0\n\tv_mbcnt_hi_u32_b32 %0, -1, %0" : "=v"(l)); return l; }
; __device__ __forceinline__ unsigned cvt_pk_bf16(float lo, float hi) { unsigned r; asm volatile("v_cvt_pk_bf16_f32 %0, %1, %2" : "=v"(r) : "v"(lo), "v"(hi)); return r; }
;     __device__ __forceinline__ void operator()(const f32x4 (&acc)[2][2][4][2], const Unit& u, int wr, int wc, int fr_, int fq_) const {
;         const int l_ = fresh_lane(), fr = l_ & 15, fq = l_ >> 4;
;         const int row0 = u.pm * BM + wr * 64 + fr, col0 = u.pn * BM + wc * 32 + 4 * fq;
; #pragma unroll
;         for (int ai = 0; ai < 2; ++ai)
; #pragma unroll
;             for (int m = 0; m < 4; ++m) { const size_t r = (size_t)(row0 + ai * HALF + m * 16); float ss = 0.f;
; #pragma unroll
;                 for (int bj = 0; bj < 2; ++bj)
; #pragma unroll
;                     for (int n = 0; n < 2; ++n) { const size_t o = r * ldc + col0 + bj * HALF + n * 16; const f32x4 c = *(const f32x4*)(R + o) + acc[ai][bj][m][n];
;                         ss += (c[0] * c[0] + c[1] * c[1]) + (c[2] * c[2] + c[3] * c[3]);
;                         u32x2 w; w.x = cvt_pk_bf16(c[0], c[1]); w.y = cvt_pk_bf16(c[2], c[3]); *(u32x2*)(HB + o) = w; }
;                 ss += __builtin_bit_cast(float, __builtin_amdgcn_ds_bpermute((l_ ^ 16) << 2, __builtin_bit_cast(int, ss)));
;                 ss += __builtin_bit_cast(float, __builtin_amdgcn_ds_bpermute((l_ ^ 32) << 2, __builtin_bit_cast(int, ss)));
;                 if (fq == 0) PSQ[r * 64 + u.pn * 4 + wc] = ss;
.LBB0_3079:
	s_or_b64 exec, exec, s[50:51]
	v_add_u32_e32 v34, 0xa0, v140
	s_waitcnt lgkmcnt(0)
	v_ashrrev_i32_e32 v35, 31, v34
	v_lshlrev_b64 v[40:41], 12, v[34:35]
	v_lshl_add_u64 v[42:43], v[40:41], 0, v[138:139]
	v_lshl_add_u64 v[44:45], v[42:43], 2, s[36:37]
	s_waitcnt vmcnt(29)
	v_mov_b64_e32 v[36:37], v[176:177]
	v_mov_b64_e32 v[38:39], v[178:179]
	v_lshl_add_u64 v[42:43], v[42:43], 1, s[14:15]
	v_pk_add_f32 v[38:39], v[32:33], v[38:39]
	v_pk_add_f32 v[36:37], v[30:31], v[36:37]
	s_nop 0
	v_cvt_pk_bf16_f32 v30, v36, v37
	v_cvt_pk_bf16_f32 v31, v38, v39
	global_store_dwordx2 v[42:43], v[30:31], off
	s_waitcnt vmcnt(29)
	v_mov_b64_e32 v[30:31], v[180:181]
	v_mov_b64_e32 v[32:33], v[182:183]
	v_lshl_add_u64 v[42:43], v[40:41], 0, v[126:127]
	v_lshl_add_u64 v[42:43], v[42:43], 1, s[14:15]
	v_mul_f32_e32 v37, v37, v37
	v_mul_f32_e32 v39, v39, v39
	v_fmac_f32_e32 v37, v36, v36
	v_fmac_f32_e32 v39, v38, v38
	v_add_f32_e32 v36, v37, v39
	v_pk_add_f32 v[32:33], v[28:29], v[32:33]
	v_pk_add_f32 v[30:31], v[26:27], v[30:31]
	s_nop 0
	v_cvt_pk_bf16_f32 v26, v30, v31
	v_cvt_pk_bf16_f32 v27, v32, v33
	global_store_dwordx2 v[42:43], v[26:27], off
	s_waitcnt vmcnt(29)
	v_mov_b64_e32 v[26:27], v[184:185]
	v_mov_b64_e32 v[28:29], v[186:187]
	v_lshl_add_u64 v[42:43], v[40:41], 0, v[122:123]
	v_lshl_add_u64 v[42:43], v[42:43], 1, s[14:15]
	v_mul_f32_e32 v31, v31, v31
	v_mul_f32_e32 v33, v33, v33
	v_fmac_f32_e32 v31, v30, v30
	v_fmac_f32_e32 v33, v32, v32
	v_add_f32_e32 v30, v31, v33
	v_add_f32_e32 v30, v36, v30
	v_pk_add_f32 v[28:29], v[24:25], v[28:29]
	v_pk_add_f32 v[26:27], v[22:23], v[26:27]
	s_nop 0
	v_cvt_pk_bf16_f32 v22, v26, v27
	v_cvt_pk_bf16_f32 v23, v28, v29
	global_store_dwordx2 v[42:43], v[22:23], off
	s_waitcnt vmcnt(29)
	v_mov_b64_e32 v[22:23], v[188:189]
	v_mov_b64_e32 v[24:25], v[190:191]
	v_mul_f32_e32 v27, v27, v27
	v_mul_f32_e32 v29, v29, v29
	v_fmac_f32_e32 v27, v26, v26
	v_fmac_f32_e32 v29, v28, v28
	v_add_f32_e32 v26, v27, v29
	v_add_f32_e32 v26, v30, v26
	v_pk_add_f32 v[20:21], v[20:21], v[24:25]
	v_pk_add_f32 v[22:23], v[18:19], v[22:23]
	v_mul_f32_e32 v19, v21, v21
	v_mul_f32_e32 v18, v23, v23
	v_fmac_f32_e32 v18, v22, v22
	v_fmac_f32_e32 v19, v20, v20
	v_add_f32_e32 v18, v18, v19
	v_add_f32_e32 v18, v26, v18
	ds_bpermute_b32 v19, v119, v18
	v_lshl_add_u64 v[24:25], v[40:41], 0, v[114:115]
	v_cvt_pk_bf16_f32 v22, v22, v23
	v_cvt_pk_bf16_f32 v23, v20, v21
	v_lshl_add_u64 v[20:21], v[24:25], 1, s[14:15]
	s_waitcnt lgkmcnt(0)
	v_add_f32_e32 v18, v18, v19
	ds_bpermute_b32 v19, v118, v18
	global_store_dwordx2 v[20:21], v[22:23], off
	s_and_saveexec_b64 s[50:51], vcc
	s_cbranch_execz .LBB0_3081
	v_lshlrev_b64 v[20:21], 8, v[34:35]
	v_lshl_add_u64 v[20:21], s[16:17], 0, v[20:21]
	v_lshl_add_u64 v[20:21], s[48:49], 2, v[20:21]
	s_lshl_b32 s12, s66, 2
	v_lshl_add_u64 v[20:21], v[20:21], 0, s[12:13]
	s_waitcnt lgkmcnt(0)
	v_add_f32_e32 v18, v18, v19
	global_store_dword v[20:21], v18, off
.LBB0_3081:
	s_or_b64 exec, exec, s[50:51]
	v_add_u32_e32 v18, 0xb0, v140
	s_waitcnt lgkmcnt(0)
	v_ashrrev_i32_e32 v19, 31, v18
	v_lshlrev_b64 v[24:25], 12, v[18:19]
	v_lshl_add_u64 v[26:27], v[24:25], 0, v[138:139]
	v_lshl_add_u64 v[28:29], v[26:27], 2, s[36:37]
	s_waitcnt vmcnt(25)
	v_mov_b64_e32 v[20:21], v[192:193]
	v_mov_b64_e32 v[22:23], v[194:195]
	v_lshl_add_u64 v[26:27], v[26:27], 1, s[14:15]
	v_pk_add_f32 v[22:23], v[16:17], v[22:23]
	v_pk_add_f32 v[20:21], v[14:15], v[20:21]
	s_nop 0
	v_cvt_pk_bf16_f32 v14, v20, v21
	v_cvt_pk_bf16_f32 v15, v22, v23
	global_store_dwordx2 v[26:27], v[14:15], off
	s_waitcnt vmcnt(25)
	v_mov_b64_e32 v[14:15], v[196:197]
	v_mov_b64_e32 v[16:17], v[198:199]
	v_lshl_add_u64 v[26:27], v[24:25], 0, v[126:127]
	v_lshl_add_u64 v[26:27], v[26:27], 1, s[14:15]
	v_mul_f32_e32 v21, v21, v21
	v_mul_f32_e32 v23, v23, v23
	v_fmac_f32_e32 v21, v20, v20
	v_fmac_f32_e32 v23, v22, v22
	v_add_f32_e32 v20, v21, v23
	v_pk_add_f32 v[16:17], v[12:13], v[16:17]
	v_pk_add_f32 v[14:15], v[10:11], v[14:15]
	s_nop 0
	v_cvt_pk_bf16_f32 v10, v14, v15
	v_cvt_pk_bf16_f32 v11, v16, v17
	global_store_dwordx2 v[26:27], v[10:11], off
	s_waitcnt vmcnt(25)
	v_mov_b64_e32 v[10:11], v[200:201]
	v_mov_b64_e32 v[12:13], v[202:203]
	v_lshl_add_u64 v[26:27], v[24:25], 0, v[122:123]
	v_lshl_add_u64 v[26:27], v[26:27], 1, s[14:15]
	v_mul_f32_e32 v15, v15, v15
	v_mul_f32_e32 v17, v17, v17
	v_fmac_f32_e32 v15, v14, v14
	v_fmac_f32_e32 v17, v16, v16
	v_add_f32_e32 v14, v15, v17
	v_add_f32_e32 v14, v20, v14
	v_pk_add_f32 v[12:13], v[8:9], v[12:13]
	v_pk_add_f32 v[10:11], v[6:7], v[10:11]
	s_nop 0
	v_cvt_pk_bf16_f32 v6, v10, v11
	v_cvt_pk_bf16_f32 v7, v12, v13
	global_store_dwordx2 v[26:27], v[6:7], off
	s_waitcnt vmcnt(25)
	v_mov_b64_e32 v[6:7], v[204:205]
	v_mov_b64_e32 v[8:9], v[206:207]
	v_mul_f32_e32 v11, v11, v11
	v_mul_f32_e32 v13, v13, v13
	v_fmac_f32_e32 v11, v10, v10
	v_fmac_f32_e32 v13, v12, v12
	v_add_f32_e32 v10, v11, v13
	v_add_f32_e32 v10, v14, v10
	v_pk_add_f32 v[4:5], v[4:5], v[8:9]
	v_pk_add_f32 v[6:7], v[2:3], v[6:7]
	v_mul_f32_e32 v3, v5, v5
	v_mul_f32_e32 v2, v7, v7
	v_fmac_f32_e32 v2, v6, v6
	v_fmac_f32_e32 v3, v4, v4
	v_add_f32_e32 v2, v2, v3
	v_add_f32_e32 v2, v10, v2
	ds_bpermute_b32 v3, v119, v2
	v_lshl_add_u64 v[8:9], v[24:25], 0, v[114:115]
	v_cvt_pk_bf16_f32 v6, v6, v7
	v_cvt_pk_bf16_f32 v7, v4, v5
	v_lshl_add_u64 v[4:5], v[8:9], 1, s[14:15]
	s_waitcnt lgkmcnt(0)
	v_add_f32_e32 v2, v2, v3
	ds_bpermute_b32 v3, v118, v2
	global_store_dwordx2 v[4:5], v[6:7], off
	s_and_saveexec_b64 s[50:51], vcc
	s_cbranch_execz .LBB0_3083
	v_lshlrev_b64 v[4:5], 8, v[18:19]
	v_lshl_add_u64 v[4:5], s[16:17], 0, v[4:5]
	v_lshl_add_u64 v[4:5], s[48:49], 2, v[4:5]
	s_lshl_b32 s12, s66, 2
	v_lshl_add_u64 v[4:5], v[4:5], 0, s[12:13]
	s_waitcnt lgkmcnt(0)
	v_add_f32_e32 v2, v2, v3
	global_store_dword v[4:5], v2, off
